# baseline (speedup 1.0000x reference)
.LBB1_38:
	global_load_dwordx4 v[140:143], v228, s[52:53] sc1
	global_load_dwordx4 v[144:147], v229, s[52:53] sc1
	global_load_dwordx4 v[148:151], v230, s[52:53] sc1
	s_waitcnt vmcnt(2)
	v_cmp_eq_u32_e32 vcc, s44, v141
	v_cmp_eq_u32_e64 s[6:7], s44, v143
	s_waitcnt vmcnt(1)
	v_cmp_eq_u32_e64 s[8:9], s44, v145
	s_and_b64 s[6:7], vcc, s[6:7]
	v_cmp_eq_u32_e64 s[10:11], s44, v147
	s_and_b64 s[6:7], s[6:7], s[8:9]
	s_waitcnt vmcnt(0)
	v_cmp_eq_u32_e64 s[12:13], s44, v149
	s_and_b64 s[6:7], s[6:7], s[10:11]
	v_cmp_eq_u32_e64 s[14:15], s44, v151
	s_and_b64 s[6:7], s[6:7], s[12:13]
	s_and_b64 s[6:7], s[6:7], s[14:15]
	s_cmp_eq_u64 s[6:7], exec
	s_cbranch_scc1 .Lp8_got
	s_add_i32 s45, s45, 1
	s_and_b32 s6, s45, 0x3ff
	s_cmp_lg_u32 s6, 0
	s_cbranch_scc1 .LBB1_38
	s_cmp_lt_u32 s45, 0x80001
	s_cbranch_scc0 .Lp9_timeout
	global_load_dword v141, v167, s[22:23] offset:4 sc1
	s_waitcnt vmcnt(0)
	v_readfirstlane_b32 s6, v141
	s_cmp_eq_u32 s6, 0
	s_cbranch_scc1 .LBB1_38
.Lp9_timeout:
	s_mov_b64 s[6:7], 0
	s_branch .LBB1_45
